# attention: waves 4-7 run at s_setprio 2 so SIMD partner waves leave lockstep (on top of LDS-read pipelining)
# speedup vs baseline: 1.0118x; 1.0005x over previous
.LBB0_1161:
	s_cmp_lt_i32 s92, 16
	s_cselect_b64 s[4:5], -1, 0
	s_cmp_gt_i32 s93, 15
	s_cselect_b64 s[6:7], -1, 0
	s_and_b64 s[4:5], s[4:5], s[6:7]
	s_andn2_b64 vcc, exec, s[4:5]
	s_cbranch_vccnz .LBB0_1239
	s_cmpk_gt_i32 s89, 0x21f
	s_cbranch_scc1 .LBB0_1189
	s_cmp_lt_u32 s88, 4
	s_cbranch_scc1 .Lmy_attprio_skip
	s_setprio 2
.Lmy_attprio_skip:
	s_add_u32 s42, s26, 0x26600000
	s_addc_u32 s43, s27, 0
	s_add_u32 s3, s26, 0x29a00000
	s_addc_u32 s35, s27, 0
	s_add_u32 s49, s26, 0x2e100000
	s_addc_u32 s52, s27, 0
	s_add_u32 s44, s26, 0x588000
	s_addc_u32 s45, s27, 0
	s_mov_b32 s47, 0
	s_movk_i32 s53, 0xc00
	s_movk_i32 s54, 0x180
	v_mov_b32_e32 v135, 0
	s_movk_i32 s55, 0x3ff
	s_movk_i32 s56, 0x3f0
	s_mov_b32 s57, 0xffff0000
	s_movk_i32 s58, 0x7fff
	s_movk_i32 s59, 0x100
	s_mov_b32 s60, 0x2aaaaaab
	s_movk_i32 s61, 0xfe80
	s_movk_i32 s62, 0x70
	s_movk_i32 s63, 0x840
	s_movk_i32 s64, 0x60
	s_mov_b32 s65, 0x42ddb3d8
	s_add_i32 s66, 0, 0x14000
	s_mov_b32 s48, 0x3dd53b94
	v_mov_b32_e32 v1, 1
	v_mov_b32_e32 v148, 0x780
	v_mov_b32_e32 v149, 0x100
	v_mov_b32_e32 v150, 0xf149f2ca
	s_mov_b32 s7, s89
	s_mov_b32 s67, 0
	s_branch .LBB0_1165

.LBB0_1189:
	s_setprio 0
	s_cmp_lt_i32 s93, 17
	s_cbranch_scc1 .LBB0_1239
	s_waitcnt vmcnt(0)
	v_cmp_eq_u32_e32 vcc, 0, v0
	s_waitcnt vmcnt(0)
	s_barrier
	s_and_saveexec_b64 s[4:5], vcc
	s_cbranch_execz .LBB0_1238
	s_add_i32 s3, 0, 0x23d60
	v_mov_b32_e32 v1, s3
	s_waitcnt vmcnt(0) expcnt(0) lgkmcnt(0)
	ds_read_b32 v3, v1
	s_add_i32 s3, 0, 0x23d64
	v_mov_b32_e32 v1, s3
	ds_read_b32 v1, v1
	s_waitcnt lgkmcnt(1)
	v_cmp_ne_u32_e32 vcc, 0, v3
	s_cbranch_vccnz .LBB0_1206
	v_readlane_b32 s6, v255, 0
	v_readlane_b32 s7, v255, 1
	s_load_dwordx2 s[10:11], s[6:7], 0x4
	v_readlane_b32 s6, v255, 4
	v_readlane_b32 s7, v255, 5
	s_lshl_b64 s[6:7], s[6:7], 2
	v_readlane_b32 s3, v255, 2
	s_add_u32 s6, s3, s6
	v_readlane_b32 s3, v255, 3
	s_addc_u32 s7, s3, s7
	s_add_u32 s8, s6, 0x1000
	s_addc_u32 s9, s7, 0
	s_waitcnt lgkmcnt(0)
	s_mul_i32 s3, s10, s34
	s_add_u32 s10, s6, 0x1100
	s_mul_i32 s3, s3, s11
	s_addc_u32 s11, s7, 0
	s_add_u32 s12, s6, 0x1200
	s_addc_u32 s13, s7, 0
	s_add_u32 s14, s6, 0x1300
	s_addc_u32 s15, s7, 0
	s_mov_b32 s22, 1
	v_mov_b32_e32 v17, 0
	s_branch .LBB0_1194
